# LDS-free expert-weight conversion with a 3-deep (24 KB per wave) load pipeline instead of 4-deep: less conversion traffic in flight beside the attention K/V stream
# baseline (speedup 1.0000x reference)
; #define GAS __attribute__((address_space(1)))
; #define LAS __attribute__((address_space(3)))
; #define LDS_WAIT() asm volatile("s_waitcnt lgkmcnt(0)" ::: "memory")
; __device__ __forceinline__ unsigned pk2(float lo, float hi) { unsigned r; asm("v_cvt_pk_bf16_f32 %0, %1, %2" : "=v"(r) : "v"(lo), "v"(hi)); return r; }
; __device__ __forceinline__ void t_store(const TItem& d, const f32x4 (&r)[8], LAS float* scr, int lane) {
; #pragma unroll
;     for (int i = 0; i < 8; ++i) *(LAS f32x4*)(scr + (8 * i + (lane >> 3)) * 32 + (((lane & 7) * 4 + 8 * i) & 31)) = r[i];
;     LDS_WAIT(); asm volatile("" ::: "memory");
;     const int c = lane >> 3, nl = lane & 7;
; #pragma unroll
;     for (int j = 0; j < 4; ++j) { const int n = nl + 8 * j; const LAS float* s = scr + (8 * c) * 32 + ((n + 8 * c) & 31);
;         v4u o; o.x = pk2(s[0 * 32], s[1 * 32]); o.y = pk2(s[2 * 32], s[3 * 32]); o.z = pk2(s[4 * 32], s[5 * 32]); o.w = pk2(s[6 * 32], s[7 * 32]);
;         __builtin_nontemporal_store(o, (GAS v4u*)(d.WT + (size_t)t_drow(d.kind, d.n0 + n) * d.K + d.k0 + 8 * c)); }
; __global__ void __launch_bounds__(512, 2) mk_fwd(Params p_unused) {
;     ...
;             for (unsigned tb = grab(); tb < NTICK; tb = grab()) {
;                 TItem a0 = decode((int)(2u * tb)); TItem a1 = a0; a1.n0 += 32;
;                 f32x4 ra[8], rb[8], rc[8], rd[8]; t_load(a0, ra, lane); t_load(a1, rb, lane);
;                 _Pragma("unroll 1") for (unsigned u = 0; u < 8u; u += 2u) {
;                     const TItem b0 = decode((int)(2u * (tb + u + 1u))); TItem b1 = b0; b1.n0 += 32;
;                     t_load(b0, rc, lane); t_load(b1, rd, lane);
;                     t_store(a0, ra, scr, lane); t_store(a1, rb, scr, lane);
;                     if (u + 2u < 8u) { a0 = decode((int)(2u * (tb + u + 2u))); a1 = a0; a1.n0 += 32; t_load(a0, ra, lane); t_load(a1, rb, lane); }
;                     t_store(b0, rc, scr, lane); t_store(b1, rd, scr, lane);
;                 }
.Lcv_go:
	global_load_dwordx4 v[54:57], v34, s[8:9] offset:0 nt
	global_load_dwordx4 v[58:61], v35, s[8:9] offset:0 nt
	global_load_dwordx4 v[62:65], v36, s[8:9] offset:0 nt
	global_load_dwordx4 v[66:69], v37, s[8:9] offset:0 nt
	global_load_dwordx4 v[70:73], v38, s[8:9] offset:0 nt
	global_load_dwordx4 v[74:77], v39, s[8:9] offset:0 nt
	global_load_dwordx4 v[78:81], v40, s[8:9] offset:0 nt
	global_load_dwordx4 v[82:85], v41, s[8:9] offset:0 nt
	global_load_dwordx4 v[86:89], v34, s[8:9] offset:128 nt
	global_load_dwordx4 v[90:93], v35, s[8:9] offset:128 nt
	global_load_dwordx4 v[94:97], v36, s[8:9] offset:128 nt
	global_load_dwordx4 v[98:101], v37, s[8:9] offset:128 nt
	global_load_dwordx4 v[102:105], v38, s[8:9] offset:128 nt
	global_load_dwordx4 v[106:109], v39, s[8:9] offset:128 nt
	global_load_dwordx4 v[110:113], v40, s[8:9] offset:128 nt
	global_load_dwordx4 v[114:117], v41, s[8:9] offset:128 nt
	global_load_dwordx4 v[118:121], v34, s[8:9] offset:256 nt
	global_load_dwordx4 v[122:125], v35, s[8:9] offset:256 nt
	global_load_dwordx4 v[126:129], v36, s[8:9] offset:256 nt
	global_load_dwordx4 v[130:133], v37, s[8:9] offset:256 nt
	global_load_dwordx4 v[134:137], v38, s[8:9] offset:256 nt
	global_load_dwordx4 v[138:141], v39, s[8:9] offset:256 nt
	global_load_dwordx4 v[142:145], v40, s[8:9] offset:256 nt
	global_load_dwordx4 v[146:149], v41, s[8:9] offset:256 nt
	s_waitcnt vmcnt(16)
	s_cmp_eq_u32 s25, 0
	s_movk_i32 s6, 0x0
	s_cmovk_i32 s6, 0x0
	s_add_u32 s6, s6, s24
	s_lshl_b32 s6, s6, s26
	s_add_u32 s14, s12, s6
	s_addc_u32 s15, s13, 0
	v_cvt_pk_bf16_f32 v46, v54, v58
	v_cvt_pk_bf16_f32 v47, v62, v66
	v_cvt_pk_bf16_f32 v48, v70, v74
	v_cvt_pk_bf16_f32 v49, v78, v82
	global_store_dwordx4 v42, v[46:49], s[14:15] nt
	v_cvt_pk_bf16_f32 v50, v55, v59
	v_cvt_pk_bf16_f32 v51, v63, v67
	v_cvt_pk_bf16_f32 v52, v71, v75
	v_cvt_pk_bf16_f32 v53, v79, v83
	global_store_dwordx4 v43, v[50:53], s[14:15] nt
	v_cvt_pk_bf16_f32 v46, v56, v60
	v_cvt_pk_bf16_f32 v47, v64, v68
	v_cvt_pk_bf16_f32 v48, v72, v76
	v_cvt_pk_bf16_f32 v49, v80, v84
	global_store_dwordx4 v44, v[46:49], s[14:15] nt
	v_cvt_pk_bf16_f32 v50, v57, v61
	v_cvt_pk_bf16_f32 v51, v65, v69
	v_cvt_pk_bf16_f32 v52, v73, v77
	v_cvt_pk_bf16_f32 v53, v81, v85
	global_store_dwordx4 v45, v[50:53], s[14:15] nt
	global_load_dwordx4 v[54:57], v34, s[8:9] offset:384 nt
	global_load_dwordx4 v[58:61], v35, s[8:9] offset:384 nt
	global_load_dwordx4 v[62:65], v36, s[8:9] offset:384 nt
	global_load_dwordx4 v[66:69], v37, s[8:9] offset:384 nt
	global_load_dwordx4 v[70:73], v38, s[8:9] offset:384 nt
	global_load_dwordx4 v[74:77], v39, s[8:9] offset:384 nt
	global_load_dwordx4 v[78:81], v40, s[8:9] offset:384 nt
	global_load_dwordx4 v[82:85], v41, s[8:9] offset:384 nt
	s_waitcnt vmcnt(20)
	s_cmp_eq_u32 s25, 0
	s_movk_i32 s6, 0x20
	s_cmovk_i32 s6, 0x20
	s_add_u32 s6, s6, s24
	s_lshl_b32 s6, s6, s26
	s_add_u32 s14, s12, s6
	s_addc_u32 s15, s13, 0
	v_cvt_pk_bf16_f32 v46, v86, v90
	v_cvt_pk_bf16_f32 v47, v94, v98
	v_cvt_pk_bf16_f32 v48, v102, v106
	v_cvt_pk_bf16_f32 v49, v110, v114
	global_store_dwordx4 v42, v[46:49], s[14:15] nt
	v_cvt_pk_bf16_f32 v50, v87, v91
	v_cvt_pk_bf16_f32 v51, v95, v99
	v_cvt_pk_bf16_f32 v52, v103, v107
	v_cvt_pk_bf16_f32 v53, v111, v115
	global_store_dwordx4 v43, v[50:53], s[14:15] nt
	v_cvt_pk_bf16_f32 v46, v88, v92
	v_cvt_pk_bf16_f32 v47, v96, v100
	v_cvt_pk_bf16_f32 v48, v104, v108
	v_cvt_pk_bf16_f32 v49, v112, v116
	global_store_dwordx4 v44, v[46:49], s[14:15] nt
	v_cvt_pk_bf16_f32 v50, v89, v93
	v_cvt_pk_bf16_f32 v51, v97, v101
	v_cvt_pk_bf16_f32 v52, v105, v109
	v_cvt_pk_bf16_f32 v53, v113, v117
	global_store_dwordx4 v45, v[50:53], s[14:15] nt
	global_load_dwordx4 v[86:89], v34, s[8:9] offset:512 nt
	global_load_dwordx4 v[90:93], v35, s[8:9] offset:512 nt
	global_load_dwordx4 v[94:97], v36, s[8:9] offset:512 nt
	global_load_dwordx4 v[98:101], v37, s[8:9] offset:512 nt
	global_load_dwordx4 v[102:105], v38, s[8:9] offset:512 nt
	global_load_dwordx4 v[106:109], v39, s[8:9] offset:512 nt
	global_load_dwordx4 v[110:113], v40, s[8:9] offset:512 nt
	global_load_dwordx4 v[114:117], v41, s[8:9] offset:512 nt
	s_waitcnt vmcnt(24)
	s_cmp_eq_u32 s25, 0
	s_movk_i32 s6, 0x40
	s_cmovk_i32 s6, 0x40
	s_add_u32 s6, s6, s24
	s_lshl_b32 s6, s6, s26
	s_add_u32 s14, s12, s6
	s_addc_u32 s15, s13, 0
	v_cvt_pk_bf16_f32 v46, v118, v122
	v_cvt_pk_bf16_f32 v47, v126, v130
	v_cvt_pk_bf16_f32 v48, v134, v138
	v_cvt_pk_bf16_f32 v49, v142, v146
	global_store_dwordx4 v42, v[46:49], s[14:15] nt
	v_cvt_pk_bf16_f32 v50, v119, v123
	v_cvt_pk_bf16_f32 v51, v127, v131
	v_cvt_pk_bf16_f32 v52, v135, v139
	v_cvt_pk_bf16_f32 v53, v143, v147
	global_store_dwordx4 v43, v[50:53], s[14:15] nt
	v_cvt_pk_bf16_f32 v46, v120, v124
	v_cvt_pk_bf16_f32 v47, v128, v132
	v_cvt_pk_bf16_f32 v48, v136, v140
	v_cvt_pk_bf16_f32 v49, v144, v148
	global_store_dwordx4 v44, v[46:49], s[14:15] nt
	v_cvt_pk_bf16_f32 v50, v121, v125
	v_cvt_pk_bf16_f32 v51, v129, v133
	v_cvt_pk_bf16_f32 v52, v137, v141
	v_cvt_pk_bf16_f32 v53, v145, v149
	global_store_dwordx4 v45, v[50:53], s[14:15] nt
	global_load_dwordx4 v[118:121], v34, s[8:9] offset:640 nt
	global_load_dwordx4 v[122:125], v35, s[8:9] offset:640 nt
	global_load_dwordx4 v[126:129], v36, s[8:9] offset:640 nt
	global_load_dwordx4 v[130:133], v37, s[8:9] offset:640 nt
	global_load_dwordx4 v[134:137], v38, s[8:9] offset:640 nt
	global_load_dwordx4 v[138:141], v39, s[8:9] offset:640 nt
	global_load_dwordx4 v[142:145], v40, s[8:9] offset:640 nt
	global_load_dwordx4 v[146:149], v41, s[8:9] offset:640 nt
	s_waitcnt vmcnt(24)
; #define GAS __attribute__((address_space(1)))
; #define LAS __attribute__((address_space(3)))
; #define LDS_WAIT() asm volatile("s_waitcnt lgkmcnt(0)" ::: "memory")
; __device__ __forceinline__ unsigned pk2(float lo, float hi) { unsigned r; asm("v_cvt_pk_bf16_f32 %0, %1, %2" : "=v"(r) : "v"(lo), "v"(hi)); return r; }
; __device__ __forceinline__ void t_store(const TItem& d, const f32x4 (&r)[8], LAS float* scr, int lane) {
; #pragma unroll
;     for (int i = 0; i < 8; ++i) *(LAS f32x4*)(scr + (8 * i + (lane >> 3)) * 32 + (((lane & 7) * 4 + 8 * i) & 31)) = r[i];
;     LDS_WAIT(); asm volatile("" ::: "memory");
;     const int c = lane >> 3, nl = lane & 7;
; #pragma unroll
;     for (int j = 0; j < 4; ++j) { const int n = nl + 8 * j; const LAS float* s = scr + (8 * c) * 32 + ((n + 8 * c) & 31);
;         v4u o; o.x = pk2(s[0 * 32], s[1 * 32]); o.y = pk2(s[2 * 32], s[3 * 32]); o.z = pk2(s[4 * 32], s[5 * 32]); o.w = pk2(s[6 * 32], s[7 * 32]);
;         __builtin_nontemporal_store(o, (GAS v4u*)(d.WT + (size_t)t_drow(d.kind, d.n0 + n) * d.K + d.k0 + 8 * c)); }
; __global__ void __launch_bounds__(512, 2) mk_fwd(Params p_unused) {
;     ...
;             for (unsigned tb = grab(); tb < NTICK; tb = grab()) {
;                 TItem a0 = decode((int)(2u * tb)); TItem a1 = a0; a1.n0 += 32;
;                 f32x4 ra[8], rb[8], rc[8], rd[8]; t_load(a0, ra, lane); t_load(a1, rb, lane);
;                 _Pragma("unroll 1") for (unsigned u = 0; u < 8u; u += 2u) {
;                     const TItem b0 = decode((int)(2u * (tb + u + 1u))); TItem b1 = b0; b1.n0 += 32;
;                     t_load(b0, rc, lane); t_load(b1, rd, lane);
;                     t_store(a0, ra, scr, lane); t_store(a1, rb, scr, lane);
;                     if (u + 2u < 8u) { a0 = decode((int)(2u * (tb + u + 2u))); a1 = a0; a1.n0 += 32; t_load(a0, ra, lane); t_load(a1, rb, lane); }
;                     t_store(b0, rc, scr, lane); t_store(b1, rd, scr, lane);
;                 }
	s_cmp_eq_u32 s25, 0
	s_movk_i32 s6, 0x60
	s_cmovk_i32 s6, 0x60
	s_add_u32 s6, s6, s24
	s_lshl_b32 s6, s6, s26
	s_add_u32 s14, s12, s6
	s_addc_u32 s15, s13, 0
	v_cvt_pk_bf16_f32 v46, v54, v58
	v_cvt_pk_bf16_f32 v47, v62, v66
	v_cvt_pk_bf16_f32 v48, v70, v74
	v_cvt_pk_bf16_f32 v49, v78, v82
	global_store_dwordx4 v42, v[46:49], s[14:15] nt
	v_cvt_pk_bf16_f32 v50, v55, v59
	v_cvt_pk_bf16_f32 v51, v63, v67
	v_cvt_pk_bf16_f32 v52, v71, v75
	v_cvt_pk_bf16_f32 v53, v79, v83
	global_store_dwordx4 v43, v[50:53], s[14:15] nt
	v_cvt_pk_bf16_f32 v46, v56, v60
	v_cvt_pk_bf16_f32 v47, v64, v68
	v_cvt_pk_bf16_f32 v48, v72, v76
	v_cvt_pk_bf16_f32 v49, v80, v84
	global_store_dwordx4 v44, v[46:49], s[14:15] nt
	v_cvt_pk_bf16_f32 v50, v57, v61
	v_cvt_pk_bf16_f32 v51, v65, v69
	v_cvt_pk_bf16_f32 v52, v73, v77
	v_cvt_pk_bf16_f32 v53, v81, v85
	global_store_dwordx4 v45, v[50:53], s[14:15] nt
	global_load_dwordx4 v[54:57], v34, s[8:9] offset:768 nt
	global_load_dwordx4 v[58:61], v35, s[8:9] offset:768 nt
	global_load_dwordx4 v[62:65], v36, s[8:9] offset:768 nt
	global_load_dwordx4 v[66:69], v37, s[8:9] offset:768 nt
	global_load_dwordx4 v[70:73], v38, s[8:9] offset:768 nt
	global_load_dwordx4 v[74:77], v39, s[8:9] offset:768 nt
	global_load_dwordx4 v[78:81], v40, s[8:9] offset:768 nt
	global_load_dwordx4 v[82:85], v41, s[8:9] offset:768 nt
	s_waitcnt vmcnt(24)
	s_cmp_eq_u32 s25, 0
	s_movk_i32 s6, 0x80
	s_cmovk_i32 s6, 0x100
	s_add_u32 s6, s6, s24
	s_lshl_b32 s6, s6, s26
	s_add_u32 s14, s12, s6
	s_addc_u32 s15, s13, 0
	v_cvt_pk_bf16_f32 v46, v86, v90
	v_cvt_pk_bf16_f32 v47, v94, v98
	v_cvt_pk_bf16_f32 v48, v102, v106
	v_cvt_pk_bf16_f32 v49, v110, v114
	global_store_dwordx4 v42, v[46:49], s[14:15] nt
	v_cvt_pk_bf16_f32 v50, v87, v91
	v_cvt_pk_bf16_f32 v51, v95, v99
	v_cvt_pk_bf16_f32 v52, v103, v107
	v_cvt_pk_bf16_f32 v53, v111, v115
	global_store_dwordx4 v43, v[50:53], s[14:15] nt
	v_cvt_pk_bf16_f32 v46, v88, v92
	v_cvt_pk_bf16_f32 v47, v96, v100
	v_cvt_pk_bf16_f32 v48, v104, v108
	v_cvt_pk_bf16_f32 v49, v112, v116
	global_store_dwordx4 v44, v[46:49], s[14:15] nt
	v_cvt_pk_bf16_f32 v50, v89, v93
	v_cvt_pk_bf16_f32 v51, v97, v101
	v_cvt_pk_bf16_f32 v52, v105, v109
	v_cvt_pk_bf16_f32 v53, v113, v117
	global_store_dwordx4 v45, v[50:53], s[14:15] nt
	global_load_dwordx4 v[86:89], v34, s[8:9] offset:896 nt
	global_load_dwordx4 v[90:93], v35, s[8:9] offset:896 nt
	global_load_dwordx4 v[94:97], v36, s[8:9] offset:896 nt
	global_load_dwordx4 v[98:101], v37, s[8:9] offset:896 nt
	global_load_dwordx4 v[102:105], v38, s[8:9] offset:896 nt
	global_load_dwordx4 v[106:109], v39, s[8:9] offset:896 nt
	global_load_dwordx4 v[110:113], v40, s[8:9] offset:896 nt
	global_load_dwordx4 v[114:117], v41, s[8:9] offset:896 nt
	s_waitcnt vmcnt(24)
	s_cmp_eq_u32 s25, 0
	s_movk_i32 s6, 0xa0
	s_cmovk_i32 s6, 0x120
	s_add_u32 s6, s6, s24
	s_lshl_b32 s6, s6, s26
	s_add_u32 s14, s12, s6
	s_addc_u32 s15, s13, 0
	v_cvt_pk_bf16_f32 v46, v118, v122
	v_cvt_pk_bf16_f32 v47, v126, v130
	v_cvt_pk_bf16_f32 v48, v134, v138
	v_cvt_pk_bf16_f32 v49, v142, v146
	global_store_dwordx4 v42, v[46:49], s[14:15] nt
	v_cvt_pk_bf16_f32 v50, v119, v123
	v_cvt_pk_bf16_f32 v51, v127, v131
	v_cvt_pk_bf16_f32 v52, v135, v139
	v_cvt_pk_bf16_f32 v53, v143, v147
	global_store_dwordx4 v43, v[50:53], s[14:15] nt
	v_cvt_pk_bf16_f32 v46, v120, v124
	v_cvt_pk_bf16_f32 v47, v128, v132
	v_cvt_pk_bf16_f32 v48, v136, v140
	v_cvt_pk_bf16_f32 v49, v144, v148
	global_store_dwordx4 v44, v[46:49], s[14:15] nt
	v_cvt_pk_bf16_f32 v50, v121, v125
	v_cvt_pk_bf16_f32 v51, v129, v133
	v_cvt_pk_bf16_f32 v52, v137, v141
	v_cvt_pk_bf16_f32 v53, v145, v149
	global_store_dwordx4 v45, v[50:53], s[14:15] nt
	global_load_dwordx4 v[118:121], v34, s[8:9] offset:1024 nt
	global_load_dwordx4 v[122:125], v35, s[8:9] offset:1024 nt
	global_load_dwordx4 v[126:129], v36, s[8:9] offset:1024 nt
	global_load_dwordx4 v[130:133], v37, s[8:9] offset:1024 nt
	global_load_dwordx4 v[134:137], v38, s[8:9] offset:1024 nt
	global_load_dwordx4 v[138:141], v39, s[8:9] offset:1024 nt
	global_load_dwordx4 v[142:145], v40, s[8:9] offset:1024 nt
	global_load_dwordx4 v[146:149], v41, s[8:9] offset:1024 nt
	s_waitcnt vmcnt(24)
	s_cmp_eq_u32 s25, 0
	s_movk_i32 s6, 0xc0
	s_cmovk_i32 s6, 0x140
	s_add_u32 s6, s6, s24
	s_lshl_b32 s6, s6, s26
	s_add_u32 s14, s12, s6
	s_addc_u32 s15, s13, 0
	v_cvt_pk_bf16_f32 v46, v54, v58
	v_cvt_pk_bf16_f32 v47, v62, v66
	v_cvt_pk_bf16_f32 v48, v70, v74
	v_cvt_pk_bf16_f32 v49, v78, v82
	global_store_dwordx4 v42, v[46:49], s[14:15] nt
	v_cvt_pk_bf16_f32 v50, v55, v59
	v_cvt_pk_bf16_f32 v51, v63, v67
	v_cvt_pk_bf16_f32 v52, v71, v75
	v_cvt_pk_bf16_f32 v53, v79, v83
	global_store_dwordx4 v43, v[50:53], s[14:15] nt
	v_cvt_pk_bf16_f32 v46, v56, v60
	v_cvt_pk_bf16_f32 v47, v64, v68
	v_cvt_pk_bf16_f32 v48, v72, v76
	v_cvt_pk_bf16_f32 v49, v80, v84
	global_store_dwordx4 v44, v[46:49], s[14:15] nt
	v_cvt_pk_bf16_f32 v50, v57, v61
	v_cvt_pk_bf16_f32 v51, v65, v69
	v_cvt_pk_bf16_f32 v52, v73, v77
	v_cvt_pk_bf16_f32 v53, v81, v85
	global_store_dwordx4 v45, v[50:53], s[14:15] nt
	global_load_dwordx4 v[54:57], v34, s[8:9] offset:1152 nt
	global_load_dwordx4 v[58:61], v35, s[8:9] offset:1152 nt
	global_load_dwordx4 v[62:65], v36, s[8:9] offset:1152 nt
	global_load_dwordx4 v[66:69], v37, s[8:9] offset:1152 nt
	global_load_dwordx4 v[70:73], v38, s[8:9] offset:1152 nt
	global_load_dwordx4 v[74:77], v39, s[8:9] offset:1152 nt
	global_load_dwordx4 v[78:81], v40, s[8:9] offset:1152 nt
	global_load_dwordx4 v[82:85], v41, s[8:9] offset:1152 nt
	s_waitcnt vmcnt(24)
; #define GAS __attribute__((address_space(1)))
; #define LAS __attribute__((address_space(3)))
; #define LDS_WAIT() asm volatile("s_waitcnt lgkmcnt(0)" ::: "memory")
; __device__ __forceinline__ unsigned pk2(float lo, float hi) { unsigned r; asm("v_cvt_pk_bf16_f32 %0, %1, %2" : "=v"(r) : "v"(lo), "v"(hi)); return r; }
; __device__ __forceinline__ void t_store(const TItem& d, const f32x4 (&r)[8], LAS float* scr, int lane) {
; #pragma unroll
;     for (int i = 0; i < 8; ++i) *(LAS f32x4*)(scr + (8 * i + (lane >> 3)) * 32 + (((lane & 7) * 4 + 8 * i) & 31)) = r[i];
;     LDS_WAIT(); asm volatile("" ::: "memory");
;     const int c = lane >> 3, nl = lane & 7;
; #pragma unroll
;     for (int j = 0; j < 4; ++j) { const int n = nl + 8 * j; const LAS float* s = scr + (8 * c) * 32 + ((n + 8 * c) & 31);
;         v4u o; o.x = pk2(s[0 * 32], s[1 * 32]); o.y = pk2(s[2 * 32], s[3 * 32]); o.z = pk2(s[4 * 32], s[5 * 32]); o.w = pk2(s[6 * 32], s[7 * 32]);
;         __builtin_nontemporal_store(o, (GAS v4u*)(d.WT + (size_t)t_drow(d.kind, d.n0 + n) * d.K + d.k0 + 8 * c)); }
; __global__ void __launch_bounds__(512, 2) mk_fwd(Params p_unused) {
;     ...
;             for (unsigned tb = grab(); tb < NTICK; tb = grab()) {
;                 TItem a0 = decode((int)(2u * tb)); TItem a1 = a0; a1.n0 += 32;
;                 f32x4 ra[8], rb[8], rc[8], rd[8]; t_load(a0, ra, lane); t_load(a1, rb, lane);
;                 _Pragma("unroll 1") for (unsigned u = 0; u < 8u; u += 2u) {
;                     const TItem b0 = decode((int)(2u * (tb + u + 1u))); TItem b1 = b0; b1.n0 += 32;
;                     t_load(b0, rc, lane); t_load(b1, rd, lane);
;                     t_store(a0, ra, scr, lane); t_store(a1, rb, scr, lane);
;                     if (u + 2u < 8u) { a0 = decode((int)(2u * (tb + u + 2u))); a1 = a0; a1.n0 += 32; t_load(a0, ra, lane); t_load(a1, rb, lane); }
;                     t_store(b0, rc, scr, lane); t_store(b1, rd, scr, lane);
;                 }
	s_cmp_eq_u32 s25, 0
	s_movk_i32 s6, 0xe0
	s_cmovk_i32 s6, 0x160
	s_add_u32 s6, s6, s24
	s_lshl_b32 s6, s6, s26
	s_add_u32 s14, s12, s6
	s_addc_u32 s15, s13, 0
	v_cvt_pk_bf16_f32 v46, v86, v90
	v_cvt_pk_bf16_f32 v47, v94, v98
	v_cvt_pk_bf16_f32 v48, v102, v106
	v_cvt_pk_bf16_f32 v49, v110, v114
	global_store_dwordx4 v42, v[46:49], s[14:15] nt
	v_cvt_pk_bf16_f32 v50, v87, v91
	v_cvt_pk_bf16_f32 v51, v95, v99
	v_cvt_pk_bf16_f32 v52, v103, v107
	v_cvt_pk_bf16_f32 v53, v111, v115
	global_store_dwordx4 v43, v[50:53], s[14:15] nt
	v_cvt_pk_bf16_f32 v46, v88, v92
	v_cvt_pk_bf16_f32 v47, v96, v100
	v_cvt_pk_bf16_f32 v48, v104, v108
	v_cvt_pk_bf16_f32 v49, v112, v116
	global_store_dwordx4 v44, v[46:49], s[14:15] nt
	v_cvt_pk_bf16_f32 v50, v89, v93
	v_cvt_pk_bf16_f32 v51, v97, v101
	v_cvt_pk_bf16_f32 v52, v105, v109
	v_cvt_pk_bf16_f32 v53, v113, v117
	global_store_dwordx4 v45, v[50:53], s[14:15] nt
	global_load_dwordx4 v[86:89], v34, s[8:9] offset:1280 nt
	global_load_dwordx4 v[90:93], v35, s[8:9] offset:1280 nt
	global_load_dwordx4 v[94:97], v36, s[8:9] offset:1280 nt
	global_load_dwordx4 v[98:101], v37, s[8:9] offset:1280 nt
	global_load_dwordx4 v[102:105], v38, s[8:9] offset:1280 nt
	global_load_dwordx4 v[106:109], v39, s[8:9] offset:1280 nt
	global_load_dwordx4 v[110:113], v40, s[8:9] offset:1280 nt
	global_load_dwordx4 v[114:117], v41, s[8:9] offset:1280 nt
	s_waitcnt vmcnt(24)
	s_cmp_eq_u32 s25, 0
	s_movk_i32 s6, 0x100
	s_cmovk_i32 s6, 0x200
	s_add_u32 s6, s6, s24
	s_lshl_b32 s6, s6, s26
	s_add_u32 s14, s12, s6
	s_addc_u32 s15, s13, 0
	v_cvt_pk_bf16_f32 v46, v118, v122
	v_cvt_pk_bf16_f32 v47, v126, v130
	v_cvt_pk_bf16_f32 v48, v134, v138
	v_cvt_pk_bf16_f32 v49, v142, v146
	global_store_dwordx4 v42, v[46:49], s[14:15] nt
	v_cvt_pk_bf16_f32 v50, v119, v123
	v_cvt_pk_bf16_f32 v51, v127, v131
	v_cvt_pk_bf16_f32 v52, v135, v139
	v_cvt_pk_bf16_f32 v53, v143, v147
	global_store_dwordx4 v43, v[50:53], s[14:15] nt
	v_cvt_pk_bf16_f32 v46, v120, v124
	v_cvt_pk_bf16_f32 v47, v128, v132
	v_cvt_pk_bf16_f32 v48, v136, v140
	v_cvt_pk_bf16_f32 v49, v144, v148
	global_store_dwordx4 v44, v[46:49], s[14:15] nt
	v_cvt_pk_bf16_f32 v50, v121, v125
	v_cvt_pk_bf16_f32 v51, v129, v133
	v_cvt_pk_bf16_f32 v52, v137, v141
	v_cvt_pk_bf16_f32 v53, v145, v149
	global_store_dwordx4 v45, v[50:53], s[14:15] nt
	global_load_dwordx4 v[118:121], v34, s[8:9] offset:1408 nt
	global_load_dwordx4 v[122:125], v35, s[8:9] offset:1408 nt
	global_load_dwordx4 v[126:129], v36, s[8:9] offset:1408 nt
	global_load_dwordx4 v[130:133], v37, s[8:9] offset:1408 nt
	global_load_dwordx4 v[134:137], v38, s[8:9] offset:1408 nt
	global_load_dwordx4 v[138:141], v39, s[8:9] offset:1408 nt
	global_load_dwordx4 v[142:145], v40, s[8:9] offset:1408 nt
	global_load_dwordx4 v[146:149], v41, s[8:9] offset:1408 nt
	s_waitcnt vmcnt(24)
	s_cmp_eq_u32 s25, 0
	s_movk_i32 s6, 0x120
	s_cmovk_i32 s6, 0x220
	s_add_u32 s6, s6, s24
	s_lshl_b32 s6, s6, s26
	s_add_u32 s14, s12, s6
	s_addc_u32 s15, s13, 0
	v_cvt_pk_bf16_f32 v46, v54, v58
	v_cvt_pk_bf16_f32 v47, v62, v66
	v_cvt_pk_bf16_f32 v48, v70, v74
	v_cvt_pk_bf16_f32 v49, v78, v82
	global_store_dwordx4 v42, v[46:49], s[14:15] nt
	v_cvt_pk_bf16_f32 v50, v55, v59
	v_cvt_pk_bf16_f32 v51, v63, v67
	v_cvt_pk_bf16_f32 v52, v71, v75
	v_cvt_pk_bf16_f32 v53, v79, v83
	global_store_dwordx4 v43, v[50:53], s[14:15] nt
	v_cvt_pk_bf16_f32 v46, v56, v60
	v_cvt_pk_bf16_f32 v47, v64, v68
	v_cvt_pk_bf16_f32 v48, v72, v76
	v_cvt_pk_bf16_f32 v49, v80, v84
	global_store_dwordx4 v44, v[46:49], s[14:15] nt
	v_cvt_pk_bf16_f32 v50, v57, v61
	v_cvt_pk_bf16_f32 v51, v65, v69
	v_cvt_pk_bf16_f32 v52, v73, v77
	v_cvt_pk_bf16_f32 v53, v81, v85
	global_store_dwordx4 v45, v[50:53], s[14:15] nt
	global_load_dwordx4 v[54:57], v34, s[8:9] offset:1536 nt
	global_load_dwordx4 v[58:61], v35, s[8:9] offset:1536 nt
	global_load_dwordx4 v[62:65], v36, s[8:9] offset:1536 nt
	global_load_dwordx4 v[66:69], v37, s[8:9] offset:1536 nt
	global_load_dwordx4 v[70:73], v38, s[8:9] offset:1536 nt
	global_load_dwordx4 v[74:77], v39, s[8:9] offset:1536 nt
	global_load_dwordx4 v[78:81], v40, s[8:9] offset:1536 nt
	global_load_dwordx4 v[82:85], v41, s[8:9] offset:1536 nt
	s_waitcnt vmcnt(24)
	s_cmp_eq_u32 s25, 0
	s_movk_i32 s6, 0x140
	s_cmovk_i32 s6, 0x240
	s_add_u32 s6, s6, s24
	s_lshl_b32 s6, s6, s26
	s_add_u32 s14, s12, s6
	s_addc_u32 s15, s13, 0
	v_cvt_pk_bf16_f32 v46, v86, v90
	v_cvt_pk_bf16_f32 v47, v94, v98
	v_cvt_pk_bf16_f32 v48, v102, v106
	v_cvt_pk_bf16_f32 v49, v110, v114
	global_store_dwordx4 v42, v[46:49], s[14:15] nt
	v_cvt_pk_bf16_f32 v50, v87, v91
	v_cvt_pk_bf16_f32 v51, v95, v99
	v_cvt_pk_bf16_f32 v52, v103, v107
	v_cvt_pk_bf16_f32 v53, v111, v115
	global_store_dwordx4 v43, v[50:53], s[14:15] nt
	v_cvt_pk_bf16_f32 v46, v88, v92
	v_cvt_pk_bf16_f32 v47, v96, v100
	v_cvt_pk_bf16_f32 v48, v104, v108
	v_cvt_pk_bf16_f32 v49, v112, v116
	global_store_dwordx4 v44, v[46:49], s[14:15] nt
	v_cvt_pk_bf16_f32 v50, v89, v93
	v_cvt_pk_bf16_f32 v51, v97, v101
	v_cvt_pk_bf16_f32 v52, v105, v109
	v_cvt_pk_bf16_f32 v53, v113, v117
	global_store_dwordx4 v45, v[50:53], s[14:15] nt
	global_load_dwordx4 v[86:89], v34, s[8:9] offset:1664 nt
	global_load_dwordx4 v[90:93], v35, s[8:9] offset:1664 nt
	global_load_dwordx4 v[94:97], v36, s[8:9] offset:1664 nt
	global_load_dwordx4 v[98:101], v37, s[8:9] offset:1664 nt
	global_load_dwordx4 v[102:105], v38, s[8:9] offset:1664 nt
	global_load_dwordx4 v[106:109], v39, s[8:9] offset:1664 nt
	global_load_dwordx4 v[110:113], v40, s[8:9] offset:1664 nt
	global_load_dwordx4 v[114:117], v41, s[8:9] offset:1664 nt
	s_waitcnt vmcnt(24)
; __global__ void __launch_bounds__(512, 2) mk_fwd(Params p_unused) {
;     ...
;             for (unsigned tb = grab(); tb < NTICK; tb = grab()) {
;                 TItem a0 = decode((int)(2u * tb)); TItem a1 = a0; a1.n0 += 32;
;                 f32x4 ra[8], rb[8], rc[8], rd[8]; t_load(a0, ra, lane); t_load(a1, rb, lane);
;                 _Pragma("unroll 1") for (unsigned u = 0; u < 8u; u += 2u) {
;                     const TItem b0 = decode((int)(2u * (tb + u + 1u))); TItem b1 = b0; b1.n0 += 32;
;                     t_load(b0, rc, lane); t_load(b1, rd, lane);
;                     t_store(a0, ra, scr, lane); t_store(a1, rb, scr, lane);
;                     if (u + 2u < 8u) { a0 = decode((int)(2u * (tb + u + 2u))); a1 = a0; a1.n0 += 32; t_load(a0, ra, lane); t_load(a1, rb, lane); }
;                     t_store(b0, rc, scr, lane); t_store(b1, rd, scr, lane);
;                 }
;             }
	s_cmp_eq_u32 s25, 0
	s_movk_i32 s6, 0x160
	s_cmovk_i32 s6, 0x260
	s_add_u32 s6, s6, s24
	s_lshl_b32 s6, s6, s26
	s_add_u32 s14, s12, s6
	s_addc_u32 s15, s13, 0
	v_cvt_pk_bf16_f32 v46, v118, v122
	v_cvt_pk_bf16_f32 v47, v126, v130
	v_cvt_pk_bf16_f32 v48, v134, v138
	v_cvt_pk_bf16_f32 v49, v142, v146
	global_store_dwordx4 v42, v[46:49], s[14:15] nt
	v_cvt_pk_bf16_f32 v50, v119, v123
	v_cvt_pk_bf16_f32 v51, v127, v131
	v_cvt_pk_bf16_f32 v52, v135, v139
	v_cvt_pk_bf16_f32 v53, v143, v147
	global_store_dwordx4 v43, v[50:53], s[14:15] nt
	v_cvt_pk_bf16_f32 v46, v120, v124
	v_cvt_pk_bf16_f32 v47, v128, v132
	v_cvt_pk_bf16_f32 v48, v136, v140
	v_cvt_pk_bf16_f32 v49, v144, v148
	global_store_dwordx4 v44, v[46:49], s[14:15] nt
	v_cvt_pk_bf16_f32 v50, v121, v125
	v_cvt_pk_bf16_f32 v51, v129, v133
	v_cvt_pk_bf16_f32 v52, v137, v141
	v_cvt_pk_bf16_f32 v53, v145, v149
	global_store_dwordx4 v45, v[50:53], s[14:15] nt
	global_load_dwordx4 v[118:121], v34, s[8:9] offset:1792 nt
	global_load_dwordx4 v[122:125], v35, s[8:9] offset:1792 nt
	global_load_dwordx4 v[126:129], v36, s[8:9] offset:1792 nt
	global_load_dwordx4 v[130:133], v37, s[8:9] offset:1792 nt
	global_load_dwordx4 v[134:137], v38, s[8:9] offset:1792 nt
	global_load_dwordx4 v[138:141], v39, s[8:9] offset:1792 nt
	global_load_dwordx4 v[142:145], v40, s[8:9] offset:1792 nt
	global_load_dwordx4 v[146:149], v41, s[8:9] offset:1792 nt
	s_waitcnt vmcnt(24)
	s_cmp_eq_u32 s25, 0
	s_movk_i32 s6, 0x180
	s_cmovk_i32 s6, 0x300
	s_add_u32 s6, s6, s24
	s_lshl_b32 s6, s6, s26
	s_add_u32 s14, s12, s6
	s_addc_u32 s15, s13, 0
	v_cvt_pk_bf16_f32 v46, v54, v58
	v_cvt_pk_bf16_f32 v47, v62, v66
	v_cvt_pk_bf16_f32 v48, v70, v74
	v_cvt_pk_bf16_f32 v49, v78, v82
	global_store_dwordx4 v42, v[46:49], s[14:15] nt
	v_cvt_pk_bf16_f32 v50, v55, v59
	v_cvt_pk_bf16_f32 v51, v63, v67
	v_cvt_pk_bf16_f32 v52, v71, v75
	v_cvt_pk_bf16_f32 v53, v79, v83
	global_store_dwordx4 v43, v[50:53], s[14:15] nt
	v_cvt_pk_bf16_f32 v46, v56, v60
	v_cvt_pk_bf16_f32 v47, v64, v68
	v_cvt_pk_bf16_f32 v48, v72, v76
	v_cvt_pk_bf16_f32 v49, v80, v84
	global_store_dwordx4 v44, v[46:49], s[14:15] nt
	v_cvt_pk_bf16_f32 v50, v57, v61
	v_cvt_pk_bf16_f32 v51, v65, v69
	v_cvt_pk_bf16_f32 v52, v73, v77
	v_cvt_pk_bf16_f32 v53, v81, v85
	global_store_dwordx4 v45, v[50:53], s[14:15] nt
	global_load_dwordx4 v[54:57], v34, s[8:9] offset:1920 nt
	global_load_dwordx4 v[58:61], v35, s[8:9] offset:1920 nt
	global_load_dwordx4 v[62:65], v36, s[8:9] offset:1920 nt
	global_load_dwordx4 v[66:69], v37, s[8:9] offset:1920 nt
	global_load_dwordx4 v[70:73], v38, s[8:9] offset:1920 nt
	global_load_dwordx4 v[74:77], v39, s[8:9] offset:1920 nt
	global_load_dwordx4 v[78:81], v40, s[8:9] offset:1920 nt
	global_load_dwordx4 v[82:85], v41, s[8:9] offset:1920 nt
	s_waitcnt vmcnt(24)
	s_cmp_eq_u32 s25, 0
	s_movk_i32 s6, 0x1a0
	s_cmovk_i32 s6, 0x320
	s_add_u32 s6, s6, s24
	s_lshl_b32 s6, s6, s26
	s_add_u32 s14, s12, s6
	s_addc_u32 s15, s13, 0
	v_cvt_pk_bf16_f32 v46, v86, v90
	v_cvt_pk_bf16_f32 v47, v94, v98
	v_cvt_pk_bf16_f32 v48, v102, v106
	v_cvt_pk_bf16_f32 v49, v110, v114
	global_store_dwordx4 v42, v[46:49], s[14:15] nt
	v_cvt_pk_bf16_f32 v50, v87, v91
	v_cvt_pk_bf16_f32 v51, v95, v99
	v_cvt_pk_bf16_f32 v52, v103, v107
	v_cvt_pk_bf16_f32 v53, v111, v115
	global_store_dwordx4 v43, v[50:53], s[14:15] nt
	v_cvt_pk_bf16_f32 v46, v88, v92
	v_cvt_pk_bf16_f32 v47, v96, v100
	v_cvt_pk_bf16_f32 v48, v104, v108
	v_cvt_pk_bf16_f32 v49, v112, v116
	global_store_dwordx4 v44, v[46:49], s[14:15] nt
	v_cvt_pk_bf16_f32 v50, v89, v93
	v_cvt_pk_bf16_f32 v51, v97, v101
	v_cvt_pk_bf16_f32 v52, v105, v109
	v_cvt_pk_bf16_f32 v53, v113, v117
	global_store_dwordx4 v45, v[50:53], s[14:15] nt
	s_waitcnt vmcnt(16)
	s_cmp_eq_u32 s25, 0
	s_movk_i32 s6, 0x1c0
	s_cmovk_i32 s6, 0x340
	s_add_u32 s6, s6, s24
	s_lshl_b32 s6, s6, s26
	s_add_u32 s14, s12, s6
	s_addc_u32 s15, s13, 0
	v_cvt_pk_bf16_f32 v46, v118, v122
	v_cvt_pk_bf16_f32 v47, v126, v130
	v_cvt_pk_bf16_f32 v48, v134, v138
	v_cvt_pk_bf16_f32 v49, v142, v146
	global_store_dwordx4 v42, v[46:49], s[14:15] nt
	v_cvt_pk_bf16_f32 v50, v119, v123
	v_cvt_pk_bf16_f32 v51, v127, v131
	v_cvt_pk_bf16_f32 v52, v135, v139
	v_cvt_pk_bf16_f32 v53, v143, v147
	global_store_dwordx4 v43, v[50:53], s[14:15] nt
	v_cvt_pk_bf16_f32 v46, v120, v124
	v_cvt_pk_bf16_f32 v47, v128, v132
	v_cvt_pk_bf16_f32 v48, v136, v140
	v_cvt_pk_bf16_f32 v49, v144, v148
	global_store_dwordx4 v44, v[46:49], s[14:15] nt
	v_cvt_pk_bf16_f32 v50, v121, v125
	v_cvt_pk_bf16_f32 v51, v129, v133
	v_cvt_pk_bf16_f32 v52, v137, v141
	v_cvt_pk_bf16_f32 v53, v145, v149
	global_store_dwordx4 v45, v[50:53], s[14:15] nt
	s_waitcnt vmcnt(8)
	s_cmp_eq_u32 s25, 0
	s_movk_i32 s6, 0x1e0
	s_cmovk_i32 s6, 0x360
	s_add_u32 s6, s6, s24
	s_lshl_b32 s6, s6, s26
	s_add_u32 s14, s12, s6
	s_addc_u32 s15, s13, 0
	v_cvt_pk_bf16_f32 v46, v54, v58
	v_cvt_pk_bf16_f32 v47, v62, v66
	v_cvt_pk_bf16_f32 v48, v70, v74
	v_cvt_pk_bf16_f32 v49, v78, v82
	global_store_dwordx4 v42, v[46:49], s[14:15] nt
	v_cvt_pk_bf16_f32 v50, v55, v59
	v_cvt_pk_bf16_f32 v51, v63, v67
	v_cvt_pk_bf16_f32 v52, v71, v75
	v_cvt_pk_bf16_f32 v53, v79, v83
	global_store_dwordx4 v43, v[50:53], s[14:15] nt
	v_cvt_pk_bf16_f32 v46, v56, v60
	v_cvt_pk_bf16_f32 v47, v64, v68
	v_cvt_pk_bf16_f32 v48, v72, v76
	v_cvt_pk_bf16_f32 v49, v80, v84
	global_store_dwordx4 v44, v[46:49], s[14:15] nt
	v_cvt_pk_bf16_f32 v50, v57, v61
	v_cvt_pk_bf16_f32 v51, v65, v69
	v_cvt_pk_bf16_f32 v52, v73, v77
	v_cvt_pk_bf16_f32 v53, v81, v85
	global_store_dwordx4 v45, v[50:53], s[14:15] nt
	v_readfirstlane_b32 s40, v7
	s_nop 3
	s_branch .Lcv_loop
